# scan: waves 4-7 prefetch chunk operands 2 ahead via registers, no per-chunk store drain
# baseline (speedup 1.0000x reference)
.LBB0_553:
	s_or_b64 exec, exec, s[4:5]
	s_ashr_i32 s10, s33, 3
	s_bfe_u32 s36, s33, 0x20001
	v_mov_b32_e32 v3, v0
	s_lshl_b32 s34, s10, 7
	s_lshl_b32 s35, s36, 5
	s_or_b32 s28, s35, s34
	v_readfirstlane_b32 s4, v3
	s_ashr_i32 s4, s4, 6
	s_add_i32 s5, s28, 0xfffffe00
	s_ashr_i32 s29, s28, 31
	s_cmpk_lt_i32 s28, 0x200
	s_cselect_b32 s13, s29, 0
	s_cselect_b32 s12, s28, s5
	s_cselect_b32 s5, s68, s58
	s_cselect_b32 s11, s3, s43
	s_lshl_b64 s[12:13], s[12:13], 16
	v_and_b32_e32 v4, 63, v3
	s_add_u32 s12, s11, s12
	s_addc_u32 s13, s5, s13
	v_lshlrev_b32_e32 v76, 4, v4
	s_ashr_i32 s5, s4, 31
	s_add_i32 s16, s4, 8
	v_lshl_add_u64 v[6:7], s[12:13], 0, v[76:77]
	s_lshl_b64 s[12:13], s[4:5], 10
	s_lshl_b32 s61, s4, 10
	s_ashr_i32 s17, s16, 31
	v_lshl_add_u64 v[8:9], v[6:7], 0, s[12:13]
	s_add_i32 s5, s61, 0
	s_mov_b32 s11, m0
	s_mov_b32 m0, s5
	s_nop 0
	global_load_lds_dwordx4 v[8:9], off
	s_mov_b32 m0, s11
	s_lshl_b64 s[14:15], s[16:17], 10
	s_lshl_b32 s62, s16, 10
	s_add_i32 s18, s4, 16
	v_lshl_add_u64 v[8:9], v[6:7], 0, s[14:15]
	s_add_i32 s11, s62, 0
	s_mov_b32 s16, m0
	s_mov_b32 m0, s11
	s_nop 0
	global_load_lds_dwordx4 v[8:9], off
	s_mov_b32 m0, s16
	s_ashr_i32 s19, s18, 31
	s_lshl_b64 s[16:17], s[18:19], 10
	s_lshl_b32 s63, s18, 10
	s_add_i32 s20, s4, 24
	v_lshl_add_u64 v[8:9], v[6:7], 0, s[16:17]
	s_add_i32 s11, s63, 0
	s_mov_b32 s18, m0
	s_mov_b32 m0, s11
	s_nop 0
	global_load_lds_dwordx4 v[8:9], off
	s_mov_b32 m0, s18
	s_ashr_i32 s21, s20, 31
	s_lshl_b64 s[18:19], s[20:21], 10
	s_lshl_b32 s69, s20, 10
	s_add_i32 s22, s4, 32
	v_lshl_add_u64 v[8:9], v[6:7], 0, s[18:19]
	s_add_i32 s11, s69, 0
	s_mov_b32 s20, m0
	s_mov_b32 m0, s11
	s_nop 0
	global_load_lds_dwordx4 v[8:9], off
	s_mov_b32 m0, s20
	s_ashr_i32 s23, s22, 31
	s_lshl_b64 s[20:21], s[22:23], 10
	s_lshl_b32 s70, s22, 10
	s_add_i32 s24, s4, 40
	v_lshl_add_u64 v[8:9], v[6:7], 0, s[20:21]
	s_add_i32 s11, s70, 0
	s_mov_b32 s22, m0
	s_mov_b32 m0, s11
	s_nop 0
	global_load_lds_dwordx4 v[8:9], off
	s_mov_b32 m0, s22
	s_ashr_i32 s25, s24, 31
	s_lshl_b64 s[22:23], s[24:25], 10
	s_lshl_b32 s71, s24, 10
	s_add_i32 s26, s4, 48
	v_lshl_add_u64 v[8:9], v[6:7], 0, s[22:23]
	s_add_i32 s11, s71, 0
	s_mov_b32 s24, m0
	s_mov_b32 m0, s11
	s_nop 0
	global_load_lds_dwordx4 v[8:9], off
	s_mov_b32 m0, s24
	s_ashr_i32 s27, s26, 31
	s_lshl_b64 s[24:25], s[26:27], 10
	s_lshl_b32 s72, s26, 10
	s_add_i32 s40, s4, 56
	v_lshl_add_u64 v[8:9], v[6:7], 0, s[24:25]
	s_add_i32 s11, s72, 0
	s_mov_b32 s26, m0
	s_mov_b32 m0, s11
	s_nop 0
	global_load_lds_dwordx4 v[8:9], off
	s_mov_b32 m0, s26
	s_ashr_i32 s41, s40, 31
	s_lshl_b32 s73, s40, 10
	s_lshl_b64 s[30:31], s[28:29], 13
	s_lshl_b64 s[26:27], s[40:41], 10
	s_add_i32 s11, s73, 0
	v_lshl_add_u64 v[6:7], v[6:7], 0, s[26:27]
	s_mov_b32 s29, m0
	s_mov_b32 m0, s11
	s_nop 0
	global_load_lds_dwordx4 v[6:7], off
	s_mov_b32 m0, s29
	s_add_u32 s11, s6, s30
	s_addc_u32 s29, s7, s31
	s_add_u32 s30, s11, s12
	s_addc_u32 s31, s29, s13
	v_lshl_add_u64 v[6:7], s[30:31], 0, v[76:77]
	s_add_i32 s5, s5, 0x10000
	s_mov_b32 s11, m0
	s_mov_b32 m0, s5
	s_nop 0
	global_load_lds_dwordx4 v[6:7], off
	s_mov_b32 m0, s11
	s_cmp_lt_i32 s4, 4
	s_cbranch_scc1 .Lscl_setup_done
	s_add_i32 s32, s28, 0xfffffe00
	s_cmpk_lt_i32 s28, 0x200
	s_cselect_b32 s82, s3, s43
	s_cselect_b32 s83, s68, s58
	s_cselect_b32 s32, s28, s32
	s_add_i32 s32, s32, 1
	s_lshl_b32 s32, s32, 16
	s_add_u32 s82, s82, s32
	s_addc_u32 s83, s83, 0
	s_add_i32 s32, s28, 1
	s_lshl_b32 s32, s32, 13
	s_add_u32 s98, s6, s32
	s_addc_u32 s99, s7, 0
	s_sub_i32 s32, s4, 4
	s_lshl_b32 s32, s32, 10
	v_add_u32_e32 v182, s32, v76
	v_add_u32_e32 v183, 0x1000, v182
	v_add_u32_e32 v184, 0x2000, v182
	v_add_u32_e32 v185, 0x3000, v182
	v_add_u32_e32 v186, 0x4000, v182
	v_add_u32_e32 v187, 0x5000, v182
	v_add_u32_e32 v188, 0x6000, v182
	v_add_u32_e32 v189, 0x7000, v182
	v_add_u32_e32 v36, 0x8000, v182
	v_add_u32_e32 v37, 0x9000, v182
	v_add_u32_e32 v38, 0xa000, v182
	v_add_u32_e32 v39, 0xb000, v182
	v_add_u32_e32 v74, 0xc000, v182
	v_add_u32_e32 v75, 0xd000, v182
	v_add_u32_e32 v117, 0xe000, v182
	v_add_u32_e32 v178, 0xf000, v182
	v_mov_b32_e32 v190, v182
	v_add_u32_e32 v191, 0x12000, v182
	v_add_u32_e32 v192, 0x10000, v182
	v_add_u32_e32 v193, 0x22000, v182
	global_load_dwordx4 v[138:141], v182, s[82:83]
	global_load_dwordx4 v[142:145], v183, s[82:83]
	global_load_dwordx4 v[146:149], v184, s[82:83]
	global_load_dwordx4 v[150:153], v185, s[82:83]
	global_load_dwordx4 v[154:157], v186, s[82:83]
	global_load_dwordx4 v[158:161], v187, s[82:83]
	global_load_dwordx4 v[162:165], v188, s[82:83]
	global_load_dwordx4 v[166:169], v189, s[82:83]
	global_load_dwordx4 v[170:173], v36, s[82:83]
	global_load_dwordx4 v[174:177], v37, s[82:83]
	global_load_dwordx4 v[42:45], v38, s[82:83]
	global_load_dwordx4 v[46:49], v39, s[82:83]
	global_load_dwordx4 v[50:53], v74, s[82:83]
	global_load_dwordx4 v[54:57], v75, s[82:83]
	global_load_dwordx4 v[58:61], v117, s[82:83]
	global_load_dwordx4 v[62:65], v178, s[82:83]
	global_load_dwordx4 v[66:69], v182, s[98:99]
	global_load_dwordx4 v[70:73], v183, s[98:99]
	s_add_u32 s82, s82, 0x10000
	s_addc_u32 s83, s83, 0
	s_add_u32 s98, s98, 0x2000
	s_addc_u32 s99, s99, 0
.Lscl_setup_done:
	v_cmp_gt_i32_e32 vcc, 32, v3
	s_and_saveexec_b64 s[30:31], vcc
	s_cbranch_execz .LBB0_555
	v_add_u32_e32 v6, s28, v3
	v_ashrrev_i32_e32 v7, 31, v6
	v_lshl_add_u64 v[6:7], v[6:7], 2, s[0:1]
	global_load_dword v5, v[6:7], off
	v_lshl_add_u32 v6, v3, 2, 0
	v_add_u32_e32 v6, 0x24000, v6
	s_waitcnt vmcnt(0)
	ds_write_b32 v6, v5

.LBB0_556:
	s_add_u32 s36, s40, 1
	s_addc_u32 s37, s41, 0
	s_add_i32 s4, s34, s40
	s_add_u32 s79, s33, s40
	s_addc_u32 s5, s76, s41
	s_add_u32 s80, s77, s40
	s_addc_u32 s41, s35, s41
	s_cmpk_lt_i32 s4, 0x1ff
	s_cselect_b32 s5, s41, s5
	s_cselect_b32 s4, s80, s79
	s_cselect_b32 s41, s68, s58
	s_cselect_b32 s79, s3, s43
	s_lshl_b64 s[4:5], s[4:5], 16
	s_add_u32 s4, s79, s4
	s_addc_u32 s5, s41, s5
	s_bitcmp1_b32 s36, 0
	s_andn2_b64 vcc, exec, s[28:29]
	s_cbranch_vccz .Lscl_done
	s_bitcmp1_b32 s40, 0
	s_cbranch_scc1 .Lscl_odd
	s_cmp_lt_u32 s40, 30
	s_cbranch_scc0 .Lscl_e_noissue
	global_load_dwordx4 v[200:203], v182, s[82:83]
	global_load_dwordx4 v[204:207], v183, s[82:83]
	global_load_dwordx4 v[208:211], v184, s[82:83]
	global_load_dwordx4 v[212:215], v185, s[82:83]
	global_load_dwordx4 v[216:219], v186, s[82:83]
	global_load_dwordx4 v[220:223], v187, s[82:83]
	global_load_dwordx4 v[224:227], v188, s[82:83]
	global_load_dwordx4 v[228:231], v189, s[82:83]
	global_load_dwordx4 v[232:235], v36, s[82:83]
	global_load_dwordx4 v[236:239], v37, s[82:83]
	global_load_dwordx4 v[240:243], v38, s[82:83]
	global_load_dwordx4 v[244:247], v39, s[82:83]
	global_load_dwordx4 v[248:251], v74, s[82:83]
	global_load_dwordx4 v[118:121], v75, s[82:83]
	global_load_dwordx4 v[122:125], v117, s[82:83]
	global_load_dwordx4 v[126:129], v178, s[82:83]
	global_load_dwordx4 v[130:133], v182, s[98:99]
	global_load_dwordx4 v[134:137], v183, s[98:99]
	s_add_u32 s82, s82, 0x10000
	s_addc_u32 s83, s83, 0
	s_add_u32 s98, s98, 0x2000
	s_addc_u32 s99, s99, 0
	s_waitcnt vmcnt(18)
	s_branch .Lscl_e_write

.Lscl_e_write:
	ds_write_b128 v191, v[138:141]
	ds_write_b128 v191, v[142:145] offset:4096
	ds_write_b128 v191, v[146:149] offset:8192
	ds_write_b128 v191, v[150:153] offset:12288
	ds_write_b128 v191, v[154:157] offset:16384
	ds_write_b128 v191, v[158:161] offset:20480
	ds_write_b128 v191, v[162:165] offset:24576
	ds_write_b128 v191, v[166:169] offset:28672
	ds_write_b128 v191, v[170:173] offset:32768
	ds_write_b128 v191, v[174:177] offset:36864
	ds_write_b128 v191, v[42:45] offset:40960
	ds_write_b128 v191, v[46:49] offset:45056
	ds_write_b128 v191, v[50:53] offset:49152
	ds_write_b128 v191, v[54:57] offset:53248
	ds_write_b128 v191, v[58:61] offset:57344
	ds_write_b128 v191, v[62:65] offset:61440
	ds_write_b128 v193, v[66:69]
	ds_write_b128 v193, v[70:73] offset:4096
	s_branch .Lscl_done
.Lscl_odd:
	s_cmp_lt_u32 s40, 30
	s_cbranch_scc0 .Lscl_o_noissue
	global_load_dwordx4 v[138:141], v182, s[82:83]
	global_load_dwordx4 v[142:145], v183, s[82:83]
	global_load_dwordx4 v[146:149], v184, s[82:83]
	global_load_dwordx4 v[150:153], v185, s[82:83]
	global_load_dwordx4 v[154:157], v186, s[82:83]
	global_load_dwordx4 v[158:161], v187, s[82:83]
	global_load_dwordx4 v[162:165], v188, s[82:83]
	global_load_dwordx4 v[166:169], v189, s[82:83]
	global_load_dwordx4 v[170:173], v36, s[82:83]
	global_load_dwordx4 v[174:177], v37, s[82:83]
	global_load_dwordx4 v[42:45], v38, s[82:83]
	global_load_dwordx4 v[46:49], v39, s[82:83]
	global_load_dwordx4 v[50:53], v74, s[82:83]
	global_load_dwordx4 v[54:57], v75, s[82:83]
	global_load_dwordx4 v[58:61], v117, s[82:83]
	global_load_dwordx4 v[62:65], v178, s[82:83]
	global_load_dwordx4 v[66:69], v182, s[98:99]
	global_load_dwordx4 v[70:73], v183, s[98:99]
	s_add_u32 s82, s82, 0x10000
	s_addc_u32 s83, s83, 0
	s_add_u32 s98, s98, 0x2000
	s_addc_u32 s99, s99, 0
	s_waitcnt vmcnt(18)
	s_branch .Lscl_o_write

.Lscl_o_write:
	ds_write_b128 v190, v[200:203]
	ds_write_b128 v190, v[204:207] offset:4096
	ds_write_b128 v190, v[208:211] offset:8192
	ds_write_b128 v190, v[212:215] offset:12288
	ds_write_b128 v190, v[216:219] offset:16384
	ds_write_b128 v190, v[220:223] offset:20480
	ds_write_b128 v190, v[224:227] offset:24576
	ds_write_b128 v190, v[228:231] offset:28672
	ds_write_b128 v190, v[232:235] offset:32768
	ds_write_b128 v190, v[236:239] offset:36864
	ds_write_b128 v190, v[240:243] offset:40960
	ds_write_b128 v190, v[244:247] offset:45056
	ds_write_b128 v190, v[248:251] offset:49152
	ds_write_b128 v190, v[118:121] offset:53248
	ds_write_b128 v190, v[122:125] offset:57344
	ds_write_b128 v190, v[126:129] offset:61440
	ds_write_b128 v192, v[130:133]
	ds_write_b128 v192, v[134:137] offset:4096
.Lscl_done:
	v_cndmask_b32_e64 v3, 0, 1, s[28:29]
	v_cmp_ne_u32_e64 s[4:5], 1, v3
	s_andn2_b64 vcc, exec, s[28:29]
	s_cbranch_vccnz .LBB0_558
	s_bitcmp1_b32 s40, 0
	s_cselect_b32 s40, 0x12000, 0
	s_add_i32 s40, s40, 0
	s_add_i32 s41, s40, s74
	v_mov_b32_e32 v3, s78
	s_add_i32 s41, s41, s75
	ds_read_b32 v88, v3
	v_add_u32_e32 v3, s41, v80
	v_add_u32_e32 v56, s40, v102
	v_add_u32_e32 v81, v3, v105
	v_add_u32_e32 v117, v56, v90
	v_add_u32_e32 v174, v56, v93
	v_add_u32_e32 v175, v56, v91
	v_add_u32_e32 v176, v56, v92
	v_add_u32_e32 v3, v3, v104
	ds_read_u16 v52, v81 offset:49152
	ds_read_u16 v53, v81 offset:49408
	ds_read_u16 v54, v81 offset:49664
	ds_read_u16 v55, v81 offset:49920
	ds_read_b128 v[68:71], v117
	ds_read_b128 v[64:67], v174
	ds_read_b128 v[60:63], v175
	ds_read_b128 v[56:59], v176
	ds_read_u16 v72, v81 offset:53248
	ds_read_u16 v73, v81 offset:53504
	ds_read_u16 v74, v81 offset:53760
	ds_read_u16 v75, v81 offset:54016
	ds_read_u16 v3, v3 offset:49152
	v_add_u32_e32 v130, s40, v101
	v_add_u32_e32 v177, v130, v90
	ds_read_b128 v[118:121], v177
	v_add_u32_e32 v178, v130, v93
	s_waitcnt lgkmcnt(1)
	v_lshlrev_b32_e32 v134, 16, v3
	ds_read_u16 v3, v81 offset:57600
	ds_read_b128 v[122:125], v178
	v_add_u32_e32 v179, v130, v91
	ds_read_b128 v[126:129], v179
	v_add_u32_e32 v180, v130, v92
	s_waitcnt lgkmcnt(2)
	v_lshlrev_b32_e32 v135, 16, v3
	ds_read_u16 v3, v81 offset:57856
	ds_read_b128 v[130:133], v180
	v_cvt_pk_bf16_f32 v36, v32, v33
	v_cvt_pk_bf16_f32 v37, v34, v35
	v_cvt_pk_bf16_f32 v38, v28, v29
	s_waitcnt lgkmcnt(1)
	v_lshlrev_b32_e32 v136, 16, v3
	ds_read_u16 v3, v81 offset:58112
	v_cvt_pk_bf16_f32 v39, v30, v31
	v_cvt_pk_bf16_f32 v40, v24, v25
	v_cvt_pk_bf16_f32 v41, v26, v27
	v_cvt_pk_bf16_f32 v42, v20, v21
	s_waitcnt lgkmcnt(0)
	v_lshlrev_b32_e32 v137, 16, v3
	v_add_u32_e32 v3, s40, v99
	v_add_u32_e32 v190, v3, v90
	v_add_u32_e32 v191, v3, v93
	v_add_u32_e32 v192, v3, v91
	v_add_u32_e32 v3, v3, v92
	ds_read_b128 v[138:141], v190
	ds_read_b128 v[142:145], v191
	ds_read_b128 v[146:149], v192
	ds_read_b128 v[150:153], v3
	ds_read_u16 v154, v81 offset:61440
	ds_read_u16 v155, v81 offset:61696
	ds_read_u16 v156, v81 offset:61952
	ds_read_u16 v81, v81 offset:62208
	ds_read_b128 v[158:161], v117 offset:12288
	ds_read_b128 v[162:165], v174 offset:12288
	ds_read_b128 v[166:169], v175 offset:12288
	ds_read_b128 v[170:173], v176 offset:12288
	v_cvt_pk_bf16_f32 v43, v22, v23
	v_cvt_pk_bf16_f32 v44, v16, v17
	v_cvt_pk_bf16_f32 v45, v18, v19
	v_cvt_pk_bf16_f32 v46, v12, v13
	v_cvt_pk_bf16_f32 v47, v14, v15
	v_cvt_pk_bf16_f32 v48, v8, v9
	v_cvt_pk_bf16_f32 v49, v10, v11
	v_cvt_pk_bf16_f32 v50, v4, v5
	v_cvt_pk_bf16_f32 v51, v6, v7
	v_lshlrev_b32_e32 v52, 16, v52
	v_lshlrev_b32_e32 v53, 16, v53
	v_lshlrev_b32_e32 v54, 16, v54
	v_lshlrev_b32_e32 v55, 16, v55
	v_lshlrev_b32_e32 v72, 16, v72
	v_lshlrev_b32_e32 v73, 16, v73
	v_lshlrev_b32_e32 v74, 16, v74
	v_lshlrev_b32_e32 v75, 16, v75
	s_waitcnt lgkmcnt(7)
	v_lshlrev_b32_e32 v154, 16, v154
	s_waitcnt lgkmcnt(6)
	v_lshlrev_b32_e32 v155, 16, v155
	s_waitcnt lgkmcnt(5)
	v_lshlrev_b32_e32 v156, 16, v156
	s_waitcnt lgkmcnt(4)
	v_lshlrev_b32_e32 v157, 16, v81
	v_mfma_f32_16x16x32_bf16 v[52:55], v[68:71], v[36:39], v[52:55]
	v_mfma_f32_16x16x32_bf16 v[52:55], v[64:67], v[40:43], v[52:55]
	v_mfma_f32_16x16x32_bf16 v[52:55], v[60:63], v[44:47], v[52:55]
	v_mfma_f32_16x16x32_bf16 v[52:55], v[56:59], v[48:51], v[52:55]
	v_mfma_f32_16x16x32_bf16 v[56:59], v[118:121], v[36:39], v[72:75]
	v_mfma_f32_16x16x32_bf16 v[56:59], v[122:125], v[40:43], v[56:59]
	v_mfma_f32_16x16x32_bf16 v[56:59], v[126:129], v[44:47], v[56:59]
	v_mfma_f32_16x16x32_bf16 v[56:59], v[130:133], v[48:51], v[56:59]
	s_add_i32 s41, s40, 0x10000
	v_add_u32_e32 v81, s41, v103
	ds_read_b128 v[60:63], v117 offset:16384
	ds_read_b128 v[64:67], v174 offset:16384
	ds_read_b128 v[68:71], v175 offset:16384
	ds_read_b128 v[72:75], v176 offset:16384
	v_add_u32_e32 v117, v81, v94
	v_add_u32_e32 v81, v81, v95
	ds_read_b128 v[118:121], v117
	ds_read_b128 v[122:125], v81
	ds_read_b128 v[126:129], v177 offset:16384
	ds_read_b128 v[130:133], v178 offset:16384
	ds_read_b128 v[174:177], v179 offset:16384
	ds_read_b128 v[178:181], v180 offset:16384
	v_add_u32_e32 v81, s41, v100
	v_add_u32_e32 v117, v81, v94
	v_add_u32_e32 v81, v81, v95
	ds_read_b128 v[182:185], v117
	ds_read_b128 v[186:189], v81
	v_mfma_f32_16x16x32_bf16 v[134:137], v[138:141], v[36:39], v[134:137]
	s_waitcnt lgkmcnt(14)
	v_mfma_f32_16x16x32_bf16 v[138:141], v[158:161], v[36:39], v[154:157]
	v_mfma_f32_16x16x32_bf16 v[134:137], v[142:145], v[40:43], v[134:137]
	v_mfma_f32_16x16x32_bf16 v[138:141], v[162:165], v[40:43], v[138:141]
	v_mfma_f32_16x16x32_bf16 v[134:137], v[146:149], v[44:47], v[134:137]
	s_waitcnt lgkmcnt(13)
	v_mfma_f32_16x16x32_bf16 v[138:141], v[166:169], v[44:47], v[138:141]
	v_mfma_f32_16x16x32_bf16 v[134:137], v[150:153], v[48:51], v[134:137]
	s_waitcnt lgkmcnt(12)
	v_mfma_f32_16x16x32_bf16 v[138:141], v[170:173], v[48:51], v[138:141]
	v_cvt_pk_bf16_f32 v52, v52, v53
	v_cvt_pk_bf16_f32 v53, v54, v55
	v_cvt_pk_bf16_f32 v54, v56, v57
	v_cvt_pk_bf16_f32 v55, v58, v59
	s_nop 1
	v_cvt_pk_bf16_f32 v56, v134, v135
	v_cvt_pk_bf16_f32 v57, v136, v137
	v_cvt_pk_bf16_f32 v58, v138, v139
	v_cvt_pk_bf16_f32 v59, v140, v141
	ds_read_b128 v[134:137], v190 offset:16384
	ds_read_b128 v[138:141], v191 offset:16384
	ds_read_b128 v[142:145], v192 offset:16384
	ds_read_b128 v[146:149], v3 offset:16384
	v_add_u32_e32 v3, s41, v98
	v_add_u32_e32 v81, v3, v94
	v_add_u32_e32 v3, v3, v95
	ds_read_b128 v[150:153], v81
	ds_read_b128 v[154:157], v3
	v_add_u32_e32 v3, s40, v97
	v_add_u32_e32 v81, v3, v90
	ds_read_b128 v[158:161], v81 offset:16384
	v_add_u32_e32 v81, v3, v93
	ds_read_b128 v[162:165], v81 offset:16384
	v_add_u32_e32 v81, v3, v91
	v_add_u32_e32 v3, v3, v92
	ds_read_b128 v[166:169], v81 offset:16384
	ds_read_b128 v[170:173], v3 offset:16384
	v_add_u32_e32 v3, s41, v96
	v_add_u32_e32 v81, v3, v94
	v_add_u32_e32 v3, v3, v95
	ds_read_b128 v[190:193], v81
	ds_read_b128 v[194:197], v3
	s_waitcnt lgkmcnt(14)
	v_mfma_f32_16x16x32_bf16 v[60:63], v[60:63], v[36:39], 0
	v_mfma_f32_16x16x32_bf16 v[60:63], v[64:67], v[40:43], v[60:63]
	v_mfma_f32_16x16x32_bf16 v[60:63], v[68:71], v[44:47], v[60:63]
	v_mfma_f32_16x16x32_bf16 v[60:63], v[72:75], v[48:51], v[60:63]
	v_mfma_f32_16x16x32_bf16 v[60:63], v[118:121], v[52:55], v[60:63]
	v_mfma_f32_16x16x32_bf16 v[64:67], v[122:125], v[56:59], v[60:63]
	v_mfma_f32_16x16x32_bf16 v[60:63], v[126:129], v[36:39], 0
	v_mfma_f32_16x16x32_bf16 v[60:63], v[130:133], v[40:43], v[60:63]
	v_mfma_f32_16x16x32_bf16 v[60:63], v[174:177], v[44:47], v[60:63]
	v_mfma_f32_16x16x32_bf16 v[60:63], v[178:181], v[48:51], v[60:63]
	s_waitcnt lgkmcnt(13)
	v_mfma_f32_16x16x32_bf16 v[60:63], v[182:185], v[52:55], v[60:63]
	s_waitcnt lgkmcnt(12)
	v_mfma_f32_16x16x32_bf16 v[60:63], v[186:189], v[56:59], v[60:63]
	v_add_u32_e32 v3, s40, v108
	v_add3_u32 v70, v3, v107, v106
	v_add3_u32 v3, v3, v109, v106
	ds_read_b64_tr_b16 v[68:69], v70 offset:32768
	ds_read_b64_tr_b16 v[70:71], v70 offset:36864
	ds_read_b64_tr_b16 v[72:73], v3 offset:32768
	ds_read_b64_tr_b16 v[74:75], v3 offset:36864
	v_add_u32_e32 v3, s40, v110
	v_add3_u32 v81, v3, v107, v106
	v_add3_u32 v3, v3, v109, v106
	ds_read_b64_tr_b16 v[118:119], v81 offset:32768
	ds_read_b64_tr_b16 v[120:121], v81 offset:36864
	ds_read_b64_tr_b16 v[122:123], v3 offset:32768
	ds_read_b64_tr_b16 v[124:125], v3 offset:36864
	v_add_u32_e32 v3, s40, v111
	v_add3_u32 v81, v3, v107, v106
	v_add3_u32 v3, v3, v109, v106
	ds_read_b64_tr_b16 v[126:127], v81 offset:32768
	ds_read_b64_tr_b16 v[128:129], v81 offset:36864
	ds_read_b64_tr_b16 v[130:131], v3 offset:32768
	ds_read_b64_tr_b16 v[132:133], v3 offset:36864
	v_add_u32_e32 v3, s40, v112
	v_add3_u32 v81, v3, v107, v106
	v_add3_u32 v3, v3, v109, v106
	ds_read_b64_tr_b16 v[174:175], v81 offset:32768
	ds_read_b64_tr_b16 v[176:177], v81 offset:36864
	ds_read_b64_tr_b16 v[178:179], v3 offset:32768
	ds_read_b64_tr_b16 v[180:181], v3 offset:36864
	s_waitcnt lgkmcnt(14)
	v_mfma_f32_16x16x32_bf16 v[134:137], v[134:137], v[36:39], 0
	v_mfma_f32_16x16x32_bf16 v[36:39], v[158:161], v[36:39], 0
	v_mfma_f32_16x16x32_bf16 v[134:137], v[138:141], v[40:43], v[134:137]
	v_mfma_f32_16x16x32_bf16 v[36:39], v[162:165], v[40:43], v[36:39]
	v_mfma_f32_16x16x32_bf16 v[134:137], v[142:145], v[44:47], v[134:137]
	v_mfma_f32_16x16x32_bf16 v[36:39], v[166:169], v[44:47], v[36:39]
	v_mfma_f32_16x16x32_bf16 v[134:137], v[146:149], v[48:51], v[134:137]
	v_mfma_f32_16x16x32_bf16 v[36:39], v[170:173], v[48:51], v[36:39]
	v_mfma_f32_16x16x32_bf16 v[134:137], v[150:153], v[52:55], v[134:137]
	v_mfma_f32_16x16x32_bf16 v[36:39], v[190:193], v[52:55], v[36:39]
	v_mfma_f32_16x16x32_bf16 v[134:137], v[154:157], v[56:59], v[134:137]
	v_mfma_f32_16x16x32_bf16 v[36:39], v[194:197], v[56:59], v[36:39]
	v_add_u32_e32 v3, s40, v113
	v_add3_u32 v42, v3, v107, v106
	v_add3_u32 v3, v3, v109, v106
	ds_read_b64_tr_b16 v[40:41], v42 offset:32768
	ds_read_b64_tr_b16 v[42:43], v42 offset:36864
	ds_read_b64_tr_b16 v[44:45], v3 offset:32768
	ds_read_b64_tr_b16 v[46:47], v3 offset:36864
	v_add_u32_e32 v3, s40, v114
	v_add3_u32 v50, v3, v107, v106
	v_add3_u32 v3, v3, v109, v106
	ds_read_b64_tr_b16 v[48:49], v50 offset:32768
	ds_read_b64_tr_b16 v[50:51], v50 offset:36864
	ds_read_b64_tr_b16 v[138:139], v3 offset:32768
	ds_read_b64_tr_b16 v[140:141], v3 offset:36864
	v_add_u32_e32 v3, s40, v115
	v_add3_u32 v81, v3, v107, v106
	v_add3_u32 v3, v3, v109, v106
	ds_read_b64_tr_b16 v[142:143], v81 offset:32768
	ds_read_b64_tr_b16 v[144:145], v81 offset:36864
	ds_read_b64_tr_b16 v[146:147], v3 offset:32768
	ds_read_b64_tr_b16 v[148:149], v3 offset:36864
	v_add_u32_e32 v3, s40, v116
	v_add3_u32 v81, v3, v107, v106
	v_add3_u32 v3, v3, v109, v106
	ds_read_b64_tr_b16 v[150:151], v81 offset:32768
	ds_read_b64_tr_b16 v[152:153], v81 offset:36864
	ds_read_b64_tr_b16 v[154:155], v3 offset:32768
	ds_read_b64_tr_b16 v[156:157], v3 offset:36864
	v_pk_mul_f32 v[34:35], v[34:35], v[88:89] op_sel_hi:[1,0]
	v_pk_mul_f32 v[32:33], v[32:33], v[88:89] op_sel_hi:[1,0]
	v_pk_mul_f32 v[30:31], v[30:31], v[88:89] op_sel_hi:[1,0]
	v_pk_mul_f32 v[28:29], v[28:29], v[88:89] op_sel_hi:[1,0]
	v_pk_mul_f32 v[26:27], v[26:27], v[88:89] op_sel_hi:[1,0]
	v_pk_mul_f32 v[24:25], v[24:25], v[88:89] op_sel_hi:[1,0]
	v_pk_mul_f32 v[22:23], v[22:23], v[88:89] op_sel_hi:[1,0]
	v_pk_mul_f32 v[20:21], v[20:21], v[88:89] op_sel_hi:[1,0]
	v_mfma_f32_16x16x32_bf16 v[32:35], v[68:71], v[52:55], v[32:35]
	s_waitcnt lgkmcnt(14)
	v_mfma_f32_16x16x32_bf16 v[28:31], v[118:121], v[52:55], v[28:31]
	v_mfma_f32_16x16x32_bf16 v[24:27], v[126:129], v[52:55], v[24:27]
	v_mfma_f32_16x16x32_bf16 v[20:23], v[174:177], v[52:55], v[20:23]
	v_mfma_f32_16x16x32_bf16 v[32:35], v[72:75], v[56:59], v[32:35]
	v_mfma_f32_16x16x32_bf16 v[28:31], v[122:125], v[56:59], v[28:31]
	v_mfma_f32_16x16x32_bf16 v[24:27], v[130:133], v[56:59], v[24:27]
	v_mfma_f32_16x16x32_bf16 v[20:23], v[178:181], v[56:59], v[20:23]
	v_mul_f32_e64 v18, v18, v88
	v_mul_f32_e64 v19, v19, v88
	v_pk_mul_f32 v[16:17], v[16:17], v[88:89] op_sel_hi:[1,0]
	v_pk_mul_f32 v[14:15], v[14:15], v[88:89] op_sel_hi:[1,0]
	v_pk_mul_f32 v[12:13], v[12:13], v[88:89] op_sel_hi:[1,0]
	v_pk_mul_f32 v[10:11], v[10:11], v[88:89] op_sel_hi:[1,0]
	v_pk_mul_f32 v[8:9], v[8:9], v[88:89] op_sel_hi:[1,0]
	v_pk_mul_f32 v[6:7], v[6:7], v[88:89] op_sel_hi:[1,0]
	v_pk_mul_f32 v[4:5], v[4:5], v[88:89] op_sel_hi:[1,0]
	v_mfma_f32_16x16x32_bf16 v[16:19], v[40:43], v[52:55], v[16:19]
	s_waitcnt lgkmcnt(10)
	v_mfma_f32_16x16x32_bf16 v[12:15], v[48:51], v[52:55], v[12:15]
	s_waitcnt lgkmcnt(6)
	v_mfma_f32_16x16x32_bf16 v[8:11], v[142:145], v[52:55], v[8:11]
	s_waitcnt lgkmcnt(2)
	v_mfma_f32_16x16x32_bf16 v[4:7], v[150:153], v[52:55], v[4:7]
	v_mfma_f32_16x16x32_bf16 v[16:19], v[44:47], v[56:59], v[16:19]
	v_mfma_f32_16x16x32_bf16 v[12:15], v[138:141], v[56:59], v[12:15]
	v_mfma_f32_16x16x32_bf16 v[8:11], v[146:149], v[56:59], v[8:11]
	s_waitcnt lgkmcnt(0)
	v_mfma_f32_16x16x32_bf16 v[4:7], v[154:157], v[56:59], v[4:7]
	v_lshl_add_u64 v[42:43], v[84:85], 0, v[82:83]
	s_mov_b32 s40, 0xbc00000
	v_add_co_u32_e32 v44, vcc, s40, v42
	s_mov_b32 s40, 0xbc01000
	s_nop 0
	v_addc_co_u32_e32 v45, vcc, 0, v43, vcc
	v_add_co_u32_e32 v42, vcc, s40, v42
	v_cvt_pk_bf16_f32 v3, v64, s0
	s_nop 0
	v_addc_co_u32_e32 v43, vcc, 0, v43, vcc
	global_store_short v[42:43], v3, off offset:-4096
	v_cvt_pk_bf16_f32 v3, v65, s0
	global_store_short v[44:45], v3, off offset:2048
	v_cvt_pk_bf16_f32 v3, v66, s0
	v_lshl_add_u64 v[40:41], v[82:83], 0, s[30:31]
	global_store_short v[42:43], v3, off
	v_cvt_pk_bf16_f32 v3, v67, s0
	global_store_short v[42:43], v3, off offset:2048
	v_or_b32_e32 v42, 0x8000, v40
	v_mov_b32_e32 v43, v41
	v_cvt_pk_bf16_f32 v3, v60, s0
	v_lshl_add_u64 v[42:43], v[78:79], 0, v[42:43]
	global_store_short v[42:43], v3, off
	v_or_b32_e32 v42, 0x8800, v40
	v_mov_b32_e32 v43, v41
	v_cvt_pk_bf16_f32 v3, v61, s0
	v_lshl_add_u64 v[42:43], v[78:79], 0, v[42:43]
	global_store_short v[42:43], v3, off
	v_or_b32_e32 v42, 0x9000, v40
	v_mov_b32_e32 v43, v41
	v_cvt_pk_bf16_f32 v3, v62, s0
	v_lshl_add_u64 v[42:43], v[78:79], 0, v[42:43]
	global_store_short v[42:43], v3, off
	v_or_b32_e32 v42, 0x9800, v40
	v_mov_b32_e32 v43, v41
	v_cvt_pk_bf16_f32 v3, v63, s0
	v_lshl_add_u64 v[42:43], v[78:79], 0, v[42:43]
	global_store_short v[42:43], v3, off
	v_or_b32_e32 v42, 0x10000, v40
	v_mov_b32_e32 v43, v41
	v_cvt_pk_bf16_f32 v3, v134, s0
	v_lshl_add_u64 v[42:43], v[78:79], 0, v[42:43]
	global_store_short v[42:43], v3, off
	v_or_b32_e32 v42, 0x10800, v40
	v_mov_b32_e32 v43, v41
	v_cvt_pk_bf16_f32 v3, v135, s0
	v_lshl_add_u64 v[42:43], v[78:79], 0, v[42:43]
	global_store_short v[42:43], v3, off
	v_or_b32_e32 v42, 0x11000, v40
	v_mov_b32_e32 v43, v41
	v_cvt_pk_bf16_f32 v3, v136, s0
	v_lshl_add_u64 v[42:43], v[78:79], 0, v[42:43]
	global_store_short v[42:43], v3, off
	v_or_b32_e32 v42, 0x11800, v40
	v_mov_b32_e32 v43, v41
	v_cvt_pk_bf16_f32 v3, v137, s0
	v_lshl_add_u64 v[42:43], v[78:79], 0, v[42:43]
	global_store_short v[42:43], v3, off
	v_or_b32_e32 v42, 0x18000, v40
	v_mov_b32_e32 v43, v41
	v_cvt_pk_bf16_f32 v3, v36, s0
	v_lshl_add_u64 v[42:43], v[78:79], 0, v[42:43]
	global_store_short v[42:43], v3, off
	v_cvt_pk_bf16_f32 v3, v37, s0
	v_or_b32_e32 v36, 0x18800, v40
	v_mov_b32_e32 v37, v41
	v_lshl_add_u64 v[36:37], v[78:79], 0, v[36:37]
	global_store_short v[36:37], v3, off
	v_or_b32_e32 v36, 0x19000, v40
	v_mov_b32_e32 v37, v41
	v_cvt_pk_bf16_f32 v3, v38, s0
	v_lshl_add_u64 v[36:37], v[78:79], 0, v[36:37]
	v_or_b32_e32 v40, 0x19800, v40
	global_store_short v[36:37], v3, off
	v_cvt_pk_bf16_f32 v3, v39, s0
	v_lshl_add_u64 v[36:37], v[78:79], 0, v[40:41]
	global_store_short v[36:37], v3, off
.LBB0_558:
	s_waitcnt lgkmcnt(0)
	s_barrier
	s_add_u32 s30, s30, 0x20000
	s_addc_u32 s31, s31, 0
	s_mov_b64 s[40:41], 0x20000
	s_add_i32 s78, s78, 4
	v_lshl_add_u64 v[84:85], v[84:85], 0, s[40:41]
	s_cmp_lg_u32 s36, 31
	v_lshl_add_u64 v[86:87], v[86:87], 0, s[8:9]
	s_cbranch_scc0 .LBB0_560
	s_mov_b64 s[40:41], s[36:37]
	s_branch .LBB0_556

	.amdhsa_kernel _Z8mega_fwd4Args
		.amdhsa_group_segment_fixed_size 0
		.amdhsa_private_segment_fixed_size 0
		.amdhsa_kernarg_size 400
		.amdhsa_user_sgpr_count 2
		.amdhsa_user_sgpr_dispatch_ptr 0
		.amdhsa_user_sgpr_queue_ptr 0
		.amdhsa_user_sgpr_kernarg_segment_ptr 1
		.amdhsa_user_sgpr_dispatch_id 0
		.amdhsa_user_sgpr_kernarg_preload_length 0
		.amdhsa_user_sgpr_kernarg_preload_offset 0
		.amdhsa_user_sgpr_private_segment_size 0
		.amdhsa_uses_dynamic_stack 0
		.amdhsa_enable_private_segment 0
		.amdhsa_system_sgpr_workgroup_id_x 1
		.amdhsa_system_sgpr_workgroup_id_y 0
		.amdhsa_system_sgpr_workgroup_id_z 0
		.amdhsa_system_sgpr_workgroup_info 0
		.amdhsa_system_vgpr_workitem_id 0
		.amdhsa_next_free_vgpr 253
		.amdhsa_next_free_sgpr 102
		.amdhsa_accum_offset 256
		.amdhsa_reserve_vcc 1
		.amdhsa_float_round_mode_32 0
		.amdhsa_float_round_mode_16_64 0
		.amdhsa_float_denorm_mode_32 3
		.amdhsa_float_denorm_mode_16_64 3
		.amdhsa_dx10_clamp 1
		.amdhsa_ieee_mode 1
		.amdhsa_fp16_overflow 0
		.amdhsa_tg_split 0
		.amdhsa_exception_fp_ieee_invalid_op 0
		.amdhsa_exception_fp_denorm_src 0
		.amdhsa_exception_fp_ieee_div_zero 0
		.amdhsa_exception_fp_ieee_overflow 0
		.amdhsa_exception_fp_ieee_underflow 0
		.amdhsa_exception_fp_ieee_inexact 0
		.amdhsa_exception_int_div_zero 0
	.end_amdhsa_kernel

amdhsa.kernels:
  - .agpr_count:     0
    .args:
      - .offset:         0
        .size:           144
        .value_kind:     by_value
      - .offset:         144
        .size:           4
        .value_kind:     hidden_block_count_x
      - .offset:         148
        .size:           4
        .value_kind:     hidden_block_count_y
      - .offset:         152
        .size:           4
        .value_kind:     hidden_block_count_z
      - .offset:         156
        .size:           2
        .value_kind:     hidden_group_size_x
      - .offset:         158
        .size:           2
        .value_kind:     hidden_group_size_y
      - .offset:         160
        .size:           2
        .value_kind:     hidden_group_size_z
      - .offset:         162
        .size:           2
        .value_kind:     hidden_remainder_x
      - .offset:         164
        .size:           2
        .value_kind:     hidden_remainder_y
      - .offset:         166
        .size:           2
        .value_kind:     hidden_remainder_z
      - .offset:         184
        .size:           8
        .value_kind:     hidden_global_offset_x
      - .offset:         192
        .size:           8
        .value_kind:     hidden_global_offset_y
      - .offset:         200
        .size:           8
        .value_kind:     hidden_global_offset_z
      - .offset:         208
        .size:           2
        .value_kind:     hidden_grid_dims
      - .offset:         264
        .size:           4
        .value_kind:     hidden_dynamic_lds_size
    .group_segment_fixed_size: 0
    .kernarg_segment_align: 8
    .kernarg_segment_size: 400
    .language:       OpenCL C
    .language_version:
      - 2
      - 0
    .max_flat_workgroup_size: 512
    .name:           _Z8mega_fwd4Args
    .private_segment_fixed_size: 0
    .sgpr_count:     108
    .sgpr_spill_count: 43
    .symbol:         _Z8mega_fwd4Args.kd
    .uniform_work_group_size: 1
    .uses_dynamic_stack: false
    .vgpr_count:     253
    .vgpr_spill_count: 0
    .wavefront_size: 64
